# speedup vs baseline: 1.0680x; 1.0071x over previous
.LBB1_55:
	v_lshrrev_b32_e32 v12, 15, v8
	v_and_b32_e32 v12, 0x1fffc, v12
	v_mov_b32_e32 v13, 1
	ds_add_rtn_u32 v55, v12, v13 offset:34816

.LBB1_88:
	s_or_b64 exec, exec, s[22:23]
	s_waitcnt lgkmcnt(0)
	v_sub_u32_e32 v12, v15, v25
	v_readfirstlane_b32 s64, v14
	s_cmp_lg_u64 s[4:5], 0
	s_cbranch_scc1 .Lput_slow
	s_cmp_le_i32 s64, 0x2000
	s_cbranch_scc0 .Lput_slow
	s_mov_b64 exec, s[42:43]
	v_lshrrev_b32_e32 v32, 15, v10
	v_and_b32_e32 v32, 0x1fffc, v32
	ds_read_b32 v32, v32 offset:35840
	s_mov_b64 exec, s[40:41]
	v_lshrrev_b32_e32 v33, 15, v28
	v_and_b32_e32 v33, 0x1fffc, v33
	ds_read_b32 v33, v33 offset:35840
	s_mov_b64 exec, s[38:39]
	v_lshrrev_b32_e32 v34, 15, v11
	v_and_b32_e32 v34, 0x1fffc, v34
	ds_read_b32 v34, v34 offset:35840
	s_mov_b64 exec, s[36:37]
	v_lshrrev_b32_e32 v35, 15, v9
	v_and_b32_e32 v35, 0x1fffc, v35
	ds_read_b32 v35, v35 offset:35840
	s_mov_b64 exec, s[34:35]
	v_lshrrev_b32_e32 v36, 15, v2
	v_and_b32_e32 v36, 0x1fffc, v36
	ds_read_b32 v36, v36 offset:35840
	s_mov_b64 exec, s[28:29]
	v_lshrrev_b32_e32 v37, 15, v27
	v_and_b32_e32 v37, 0x1fffc, v37
	ds_read_b32 v37, v37 offset:35840
	s_mov_b64 exec, s[26:27]
	v_lshrrev_b32_e32 v38, 15, v3
	v_and_b32_e32 v38, 0x1fffc, v38
	ds_read_b32 v38, v38 offset:35840
	s_mov_b64 exec, s[24:25]
	v_lshrrev_b32_e32 v39, 15, v26
	v_and_b32_e32 v39, 0x1fffc, v39
	ds_read_b32 v39, v39 offset:35840
	s_waitcnt lgkmcnt(0)
	s_mov_b64 exec, s[42:43]
	v_add_u32_e32 v32, v32, v40
	v_lshlrev_b32_e32 v32, 2, v32
	v_and_b32_e32 v40, 0x1ffff, v10
	ds_write_b32 v32, v40
	s_mov_b64 exec, s[40:41]
	v_add_u32_e32 v33, v33, v41
	v_lshlrev_b32_e32 v33, 2, v33
	v_and_b32_e32 v41, 0x1ffff, v28
	ds_write_b32 v33, v41
	s_mov_b64 exec, s[38:39]
	v_add_u32_e32 v34, v34, v42
	v_lshlrev_b32_e32 v34, 2, v34
	v_and_b32_e32 v42, 0x1ffff, v11
	ds_write_b32 v34, v42
	s_mov_b64 exec, s[36:37]
	v_add_u32_e32 v35, v35, v43
	v_lshlrev_b32_e32 v35, 2, v35
	v_and_b32_e32 v43, 0x1ffff, v9
	ds_write_b32 v35, v43
	s_mov_b64 exec, s[34:35]
	v_add_u32_e32 v36, v36, v44
	v_lshlrev_b32_e32 v36, 2, v36
	v_and_b32_e32 v44, 0x1ffff, v2
	ds_write_b32 v36, v44
	s_mov_b64 exec, s[28:29]
	v_add_u32_e32 v37, v37, v45
	v_lshlrev_b32_e32 v37, 2, v37
	v_and_b32_e32 v45, 0x1ffff, v27
	ds_write_b32 v37, v45
	s_mov_b64 exec, s[26:27]
	v_add_u32_e32 v38, v38, v46
	v_lshlrev_b32_e32 v38, 2, v38
	v_and_b32_e32 v46, 0x1ffff, v3
	ds_write_b32 v38, v46
	s_mov_b64 exec, s[24:25]
	v_add_u32_e32 v39, v39, v47
	v_lshlrev_b32_e32 v39, 2, v39
	v_and_b32_e32 v47, 0x1ffff, v26
	ds_write_b32 v39, v47
	s_mov_b64 exec, s[20:21]
	v_lshrrev_b32_e32 v32, 15, v4
	v_and_b32_e32 v32, 0x1fffc, v32
	ds_read_b32 v32, v32 offset:35840
	s_mov_b64 exec, s[18:19]
	v_lshrrev_b32_e32 v33, 15, v19
	v_and_b32_e32 v33, 0x1fffc, v33
	ds_read_b32 v33, v33 offset:35840
	s_mov_b64 exec, s[16:17]
	v_lshrrev_b32_e32 v34, 15, v5
	v_and_b32_e32 v34, 0x1fffc, v34
	ds_read_b32 v34, v34 offset:35840
	s_mov_b64 exec, s[14:15]
	v_lshrrev_b32_e32 v35, 15, v18
	v_and_b32_e32 v35, 0x1fffc, v35
	ds_read_b32 v35, v35 offset:35840
	s_mov_b64 exec, s[12:13]
	v_lshrrev_b32_e32 v36, 15, v6
	v_and_b32_e32 v36, 0x1fffc, v36
	ds_read_b32 v36, v36 offset:35840
	s_mov_b64 exec, s[10:11]
	v_lshrrev_b32_e32 v37, 15, v17
	v_and_b32_e32 v37, 0x1fffc, v37
	ds_read_b32 v37, v37 offset:35840
	s_mov_b64 exec, s[8:9]
	v_lshrrev_b32_e32 v38, 15, v7
	v_and_b32_e32 v38, 0x1fffc, v38
	ds_read_b32 v38, v38 offset:35840
	s_mov_b64 exec, s[6:7]
	v_lshrrev_b32_e32 v39, 15, v8
	v_and_b32_e32 v39, 0x1fffc, v39
	ds_read_b32 v39, v39 offset:35840
	s_waitcnt lgkmcnt(0)
	s_mov_b64 exec, s[20:21]
	v_add_u32_e32 v32, v32, v48
	v_lshlrev_b32_e32 v32, 2, v32
	v_and_b32_e32 v48, 0x1ffff, v4
	ds_write_b32 v32, v48
	s_mov_b64 exec, s[18:19]
	v_add_u32_e32 v33, v33, v49
	v_lshlrev_b32_e32 v33, 2, v33
	v_and_b32_e32 v49, 0x1ffff, v19
	ds_write_b32 v33, v49
	s_mov_b64 exec, s[16:17]
	v_add_u32_e32 v34, v34, v50
	v_lshlrev_b32_e32 v34, 2, v34
	v_and_b32_e32 v50, 0x1ffff, v5
	ds_write_b32 v34, v50
	s_mov_b64 exec, s[14:15]
	v_add_u32_e32 v35, v35, v51
	v_lshlrev_b32_e32 v35, 2, v35
	v_and_b32_e32 v51, 0x1ffff, v18
	ds_write_b32 v35, v51
	s_mov_b64 exec, s[12:13]
	v_add_u32_e32 v36, v36, v52
	v_lshlrev_b32_e32 v36, 2, v36
	v_and_b32_e32 v52, 0x1ffff, v6
	ds_write_b32 v36, v52
	s_mov_b64 exec, s[10:11]
	v_add_u32_e32 v37, v37, v53
	v_lshlrev_b32_e32 v37, 2, v37
	v_and_b32_e32 v53, 0x1ffff, v17
	ds_write_b32 v37, v53
	s_mov_b64 exec, s[8:9]
	v_add_u32_e32 v38, v38, v54
	v_lshlrev_b32_e32 v38, 2, v38
	v_and_b32_e32 v54, 0x1ffff, v7
	ds_write_b32 v38, v54
	s_mov_b64 exec, s[6:7]
	v_add_u32_e32 v39, v39, v55
	v_lshlrev_b32_e32 v39, 2, v39
	v_and_b32_e32 v55, 0x1ffff, v8
	ds_write_b32 v39, v55
	s_mov_b64 exec, -1
	s_branch .LBB1_231
.Lput_slow:
	s_and_saveexec_b64 s[22:23], s[42:43]
	s_cbranch_execz .LBB1_96
	v_lshrrev_b32_e32 v13, 15, v10
	v_and_b32_e32 v13, 0x1fffc, v13
	v_mov_b32_e32 v29, 1
	ds_read_b32 v15, v13 offset:35840
	ds_add_rtn_u32 v13, v13, v29 offset:37888
	v_and_b32_e32 v10, 0x1ffff, v10
	s_waitcnt lgkmcnt(0)
	v_add_u32_e32 v13, v13, v15
	v_cmp_ge_i32_e32 vcc, v13, v25
	s_and_saveexec_b64 s[30:31], vcc
	s_xor_b64 s[30:31], exec, s[30:31]
	s_cbranch_execz .LBB1_91
	v_add_u32_e32 v30, v12, v13
	v_ashrrev_i32_e32 v31, 31, v30
	v_lshl_add_u64 v[30:31], v[30:31], 2, s[52:53]
	global_store_dword v[30:31], v10, off

.LBB1_247:
	v_lshrrev_b32_e32 v12, 15, v10
	v_and_b32_e32 v12, 0x1fffc, v12
	v_mov_b32_e32 v13, 1
	ds_add_rtn_u32 v40, v12, v13 offset:34816
	s_or_b64 exec, exec, s[4:5]
	v_cmp_ne_u32_e64 s[40:41], -1, v28
	s_and_saveexec_b64 s[4:5], s[40:41]
	s_cbranch_execz .LBB1_41
.LBB1_248:
	v_lshrrev_b32_e32 v12, 15, v28
	v_and_b32_e32 v12, 0x1fffc, v12
	v_mov_b32_e32 v13, 1
	ds_add_rtn_u32 v41, v12, v13 offset:34816
	s_or_b64 exec, exec, s[4:5]
	v_cmp_ne_u32_e64 s[38:39], -1, v11
	s_and_saveexec_b64 s[4:5], s[38:39]
	s_cbranch_execz .LBB1_42
.LBB1_249:
	v_lshrrev_b32_e32 v12, 15, v11
	v_and_b32_e32 v12, 0x1fffc, v12
	v_mov_b32_e32 v13, 1
	ds_add_rtn_u32 v42, v12, v13 offset:34816
	s_or_b64 exec, exec, s[4:5]
	s_waitcnt vmcnt(0)
	v_cmp_ne_u32_e64 s[36:37], -1, v9
	s_and_saveexec_b64 s[4:5], s[36:37]
	s_cbranch_execz .LBB1_43
.LBB1_250:
	v_lshrrev_b32_e32 v12, 15, v9
	v_and_b32_e32 v12, 0x1fffc, v12
	v_mov_b32_e32 v13, 1
	ds_add_rtn_u32 v43, v12, v13 offset:34816
	s_or_b64 exec, exec, s[4:5]
	v_cmp_ne_u32_e64 s[34:35], -1, v2
	s_and_saveexec_b64 s[4:5], s[34:35]
	s_cbranch_execz .LBB1_44
.LBB1_251:
	v_lshrrev_b32_e32 v12, 15, v2
	v_and_b32_e32 v12, 0x1fffc, v12
	v_mov_b32_e32 v13, 1
	ds_add_rtn_u32 v44, v12, v13 offset:34816
	s_or_b64 exec, exec, s[4:5]
	v_cmp_ne_u32_e64 s[28:29], -1, v27
	s_and_saveexec_b64 s[4:5], s[28:29]
	s_cbranch_execz .LBB1_45
.LBB1_252:
	v_lshrrev_b32_e32 v12, 15, v27
	v_and_b32_e32 v12, 0x1fffc, v12
	v_mov_b32_e32 v13, 1
	ds_add_rtn_u32 v45, v12, v13 offset:34816
	s_or_b64 exec, exec, s[4:5]
	v_cmp_ne_u32_e64 s[26:27], -1, v3
	s_and_saveexec_b64 s[4:5], s[26:27]
	s_cbranch_execz .LBB1_46
.LBB1_253:
	v_lshrrev_b32_e32 v12, 15, v3
	v_and_b32_e32 v12, 0x1fffc, v12
	v_mov_b32_e32 v13, 1
	ds_add_rtn_u32 v46, v12, v13 offset:34816
	s_or_b64 exec, exec, s[4:5]
	v_cmp_ne_u32_e64 s[24:25], -1, v26
	s_and_saveexec_b64 s[4:5], s[24:25]
	s_cbranch_execz .LBB1_47
.LBB1_254:
	v_lshrrev_b32_e32 v12, 15, v26
	v_and_b32_e32 v12, 0x1fffc, v12
	v_mov_b32_e32 v13, 1
	ds_add_rtn_u32 v47, v12, v13 offset:34816
	s_or_b64 exec, exec, s[4:5]
	v_cmp_ne_u32_e64 s[20:21], -1, v4
	s_and_saveexec_b64 s[4:5], s[20:21]
	s_cbranch_execz .LBB1_48
.LBB1_255:
	v_lshrrev_b32_e32 v12, 15, v4
	v_and_b32_e32 v12, 0x1fffc, v12
	v_mov_b32_e32 v13, 1
	ds_add_rtn_u32 v48, v12, v13 offset:34816
	s_or_b64 exec, exec, s[4:5]
	v_cmp_ne_u32_e64 s[18:19], -1, v19
	s_and_saveexec_b64 s[4:5], s[18:19]
	s_cbranch_execz .LBB1_49
.LBB1_256:
	v_lshrrev_b32_e32 v12, 15, v19
	v_and_b32_e32 v12, 0x1fffc, v12
	v_mov_b32_e32 v13, 1
	ds_add_rtn_u32 v49, v12, v13 offset:34816
	s_or_b64 exec, exec, s[4:5]
	v_cmp_ne_u32_e64 s[16:17], -1, v5
	s_and_saveexec_b64 s[4:5], s[16:17]
	s_cbranch_execz .LBB1_50
.LBB1_257:
	v_lshrrev_b32_e32 v12, 15, v5
	v_and_b32_e32 v12, 0x1fffc, v12
	v_mov_b32_e32 v13, 1
	ds_add_rtn_u32 v50, v12, v13 offset:34816
	s_or_b64 exec, exec, s[4:5]
	v_cmp_ne_u32_e64 s[14:15], -1, v18
	s_and_saveexec_b64 s[4:5], s[14:15]
	s_cbranch_execz .LBB1_51
.LBB1_258:
	v_lshrrev_b32_e32 v12, 15, v18
	v_and_b32_e32 v12, 0x1fffc, v12
	v_mov_b32_e32 v13, 1
	ds_add_rtn_u32 v51, v12, v13 offset:34816
	s_or_b64 exec, exec, s[4:5]
	v_cmp_ne_u32_e64 s[12:13], -1, v6
	s_and_saveexec_b64 s[4:5], s[12:13]
	s_cbranch_execz .LBB1_52
.LBB1_259:
	v_lshrrev_b32_e32 v12, 15, v6
	v_and_b32_e32 v12, 0x1fffc, v12
	v_mov_b32_e32 v13, 1
	ds_add_rtn_u32 v52, v12, v13 offset:34816
	s_or_b64 exec, exec, s[4:5]
	v_cmp_ne_u32_e64 s[10:11], -1, v17
	s_and_saveexec_b64 s[4:5], s[10:11]
	s_cbranch_execz .LBB1_53
.LBB1_260:
	v_lshrrev_b32_e32 v12, 15, v17
	v_and_b32_e32 v12, 0x1fffc, v12
	v_mov_b32_e32 v13, 1
	ds_add_rtn_u32 v53, v12, v13 offset:34816
	s_or_b64 exec, exec, s[4:5]
	v_cmp_ne_u32_e64 s[8:9], -1, v7
	s_and_saveexec_b64 s[4:5], s[8:9]
	s_cbranch_execz .LBB1_54
.LBB1_261:
	v_lshrrev_b32_e32 v12, 15, v7
	v_and_b32_e32 v12, 0x1fffc, v12
	v_mov_b32_e32 v13, 1
	ds_add_rtn_u32 v54, v12, v13 offset:34816
	s_or_b64 exec, exec, s[4:5]
	v_cmp_ne_u32_e64 s[6:7], -1, v8
	s_and_saveexec_b64 s[4:5], s[6:7]
	s_cbranch_execnz .LBB1_55
	s_branch .LBB1_56

	.amdhsa_kernel _Z5k_csrPKjPKiS2_PiPKfPfPDF16_S3_S3_S3_S5_S5_S5_S5_S7_S6_
		.amdhsa_group_segment_fixed_size 38940
		.amdhsa_private_segment_fixed_size 0
		.amdhsa_kernarg_size 128
		.amdhsa_user_sgpr_count 2
		.amdhsa_user_sgpr_dispatch_ptr 0
		.amdhsa_user_sgpr_queue_ptr 0
		.amdhsa_user_sgpr_kernarg_segment_ptr 1
		.amdhsa_user_sgpr_dispatch_id 0
		.amdhsa_user_sgpr_kernarg_preload_length 0
		.amdhsa_user_sgpr_kernarg_preload_offset 0
		.amdhsa_user_sgpr_private_segment_size 0
		.amdhsa_uses_dynamic_stack 0
		.amdhsa_enable_private_segment 0
		.amdhsa_system_sgpr_workgroup_id_x 1
		.amdhsa_system_sgpr_workgroup_id_y 0
		.amdhsa_system_sgpr_workgroup_id_z 0
		.amdhsa_system_sgpr_workgroup_info 0
		.amdhsa_system_vgpr_workitem_id 0
		.amdhsa_next_free_vgpr 64
		.amdhsa_next_free_sgpr 66
		.amdhsa_accum_offset 64
		.amdhsa_reserve_vcc 1
		.amdhsa_float_round_mode_32 0
		.amdhsa_float_round_mode_16_64 0
		.amdhsa_float_denorm_mode_32 3
		.amdhsa_float_denorm_mode_16_64 3
		.amdhsa_dx10_clamp 1
		.amdhsa_ieee_mode 1
		.amdhsa_fp16_overflow 0
		.amdhsa_tg_split 0
		.amdhsa_exception_fp_ieee_invalid_op 0
		.amdhsa_exception_fp_denorm_src 0
		.amdhsa_exception_fp_ieee_div_zero 0
		.amdhsa_exception_fp_ieee_overflow 0
		.amdhsa_exception_fp_ieee_underflow 0
		.amdhsa_exception_fp_ieee_inexact 0
		.amdhsa_exception_int_div_zero 0
	.end_amdhsa_kernel

amdhsa.kernels:
  - .agpr_count:     0
    .args:
      - .actual_access:  read_only
        .address_space:  global
        .offset:         0
        .size:           8
        .value_kind:     global_buffer
      - .actual_access:  read_only
        .address_space:  global
        .offset:         8
        .size:           8
        .value_kind:     global_buffer
      - .actual_access:  write_only
        .address_space:  global
        .offset:         16
        .size:           8
        .value_kind:     global_buffer
      - .actual_access:  read_only
        .address_space:  global
        .offset:         24
        .size:           8
        .value_kind:     global_buffer
      - .actual_access:  write_only
        .address_space:  global
        .offset:         32
        .size:           8
        .value_kind:     global_buffer
      - .actual_access:  write_only
        .address_space:  global
        .offset:         40
        .size:           8
        .value_kind:     global_buffer
      - .actual_access:  read_only
        .address_space:  global
        .offset:         48
        .size:           8
        .value_kind:     global_buffer
      - .actual_access:  read_only
        .address_space:  global
        .offset:         56
        .size:           8
        .value_kind:     global_buffer
      - .actual_access:  write_only
        .address_space:  global
        .offset:         64
        .size:           8
        .value_kind:     global_buffer
    .group_segment_fixed_size: 53904
    .kernarg_segment_align: 8
    .kernarg_segment_size: 72
    .language:       OpenCL C
    .language_version:
      - 2
      - 0
    .max_flat_workgroup_size: 1024
    .name:           _Z6k_partPKiS0_PiS1_PjS1_PKfS4_Pf
    .private_segment_fixed_size: 0
    .sgpr_count:     31
    .sgpr_spill_count: 0
    .symbol:         _Z6k_partPKiS0_PiS1_PjS1_PKfS4_Pf.kd
    .uniform_work_group_size: 1
    .uses_dynamic_stack: false
    .vgpr_count:     64
    .vgpr_spill_count: 0
    .wavefront_size: 64
  - .agpr_count:     0
    .args:
      - .actual_access:  read_only
        .address_space:  global
        .offset:         0
        .size:           8
        .value_kind:     global_buffer
      - .actual_access:  read_only
        .address_space:  global
        .offset:         8
        .size:           8
        .value_kind:     global_buffer
      - .actual_access:  read_only
        .address_space:  global
        .offset:         16
        .size:           8
        .value_kind:     global_buffer
      - .address_space:  global
        .offset:         24
        .size:           8
        .value_kind:     global_buffer
      - .actual_access:  read_only
        .address_space:  global
        .offset:         32
        .size:           8
        .value_kind:     global_buffer
      - .actual_access:  write_only
        .address_space:  global
        .offset:         40
        .size:           8
        .value_kind:     global_buffer
      - .actual_access:  write_only
        .address_space:  global
        .offset:         48
        .size:           8
        .value_kind:     global_buffer
      - .actual_access:  write_only
        .address_space:  global
        .offset:         56
        .size:           8
        .value_kind:     global_buffer
      - .actual_access:  write_only
        .address_space:  global
        .offset:         64
        .size:           8
        .value_kind:     global_buffer
      - .actual_access:  write_only
        .address_space:  global
        .offset:         72
        .size:           8
        .value_kind:     global_buffer
      - .actual_access:  read_only
        .address_space:  global
        .offset:         80
        .size:           8
        .value_kind:     global_buffer
      - .actual_access:  read_only
        .address_space:  global
        .offset:         88
        .size:           8
        .value_kind:     global_buffer
      - .actual_access:  read_only
        .address_space:  global
        .offset:         96
        .size:           8
        .value_kind:     global_buffer
      - .actual_access:  read_only
        .address_space:  global
        .offset:         104
        .size:           8
        .value_kind:     global_buffer
      - .actual_access:  write_only
        .address_space:  global
        .offset:         112
        .size:           8
        .value_kind:     global_buffer
      - .actual_access:  write_only
        .address_space:  global
        .offset:         120
        .size:           8
        .value_kind:     global_buffer
    .group_segment_fixed_size: 38940
    .kernarg_segment_align: 8
    .kernarg_segment_size: 128
    .language:       OpenCL C
    .language_version:
      - 2
      - 0
    .max_flat_workgroup_size: 1024
    .name:           _Z5k_csrPKjPKiS2_PiPKfPfPDF16_S3_S3_S3_S5_S5_S5_S5_S7_S6_
    .private_segment_fixed_size: 0
    .sgpr_count:     72
    .sgpr_spill_count: 0
    .symbol:         _Z5k_csrPKjPKiS2_PiPKfPfPDF16_S3_S3_S3_S5_S5_S5_S5_S7_S6_.kd
    .uniform_work_group_size: 1
    .uses_dynamic_stack: false
    .vgpr_count:     64
    .vgpr_spill_count: 0
    .wavefront_size: 64
  - .agpr_count:     0
    .args:
      - .actual_access:  read_only
        .address_space:  global
        .offset:         0
        .size:           8
        .value_kind:     global_buffer
      - .actual_access:  read_only
        .address_space:  global
        .offset:         8
        .size:           8
        .value_kind:     global_buffer
      - .actual_access:  read_only
        .address_space:  global
        .offset:         16
        .size:           8
        .value_kind:     global_buffer
      - .actual_access:  read_only
        .address_space:  global
        .offset:         24
        .size:           8
        .value_kind:     global_buffer
      - .actual_access:  read_only
        .address_space:  global
        .offset:         32
        .size:           8
        .value_kind:     global_buffer
      - .actual_access:  read_only
        .address_space:  global
        .offset:         40
        .size:           8
        .value_kind:     global_buffer
      - .actual_access:  write_only
        .address_space:  global
        .offset:         48
        .size:           8
        .value_kind:     global_buffer
      - .offset:         56
        .size:           4
        .value_kind:     hidden_block_count_x
      - .offset:         60
        .size:           4
        .value_kind:     hidden_block_count_y
      - .offset:         64
        .size:           4
        .value_kind:     hidden_block_count_z
      - .offset:         68
        .size:           2
        .value_kind:     hidden_group_size_x
      - .offset:         70
        .size:           2
        .value_kind:     hidden_group_size_y
      - .offset:         72
        .size:           2
        .value_kind:     hidden_group_size_z
      - .offset:         74
        .size:           2
        .value_kind:     hidden_remainder_x
      - .offset:         76
        .size:           2
        .value_kind:     hidden_remainder_y
      - .offset:         78
        .size:           2
        .value_kind:     hidden_remainder_z
      - .offset:         96
        .size:           8
        .value_kind:     hidden_global_offset_x
      - .offset:         104
        .size:           8
        .value_kind:     hidden_global_offset_y
      - .offset:         112
        .size:           8
        .value_kind:     hidden_global_offset_z
      - .offset:         120
        .size:           2
        .value_kind:     hidden_grid_dims
    .group_segment_fixed_size: 32768
    .kernarg_segment_align: 8
    .kernarg_segment_size: 312
    .language:       OpenCL C
    .language_version:
      - 2
      - 0
    .max_flat_workgroup_size: 256
    .name:           _Z5k_decPKiPKDF16_S2_PKfS4_S4_Pf
    .private_segment_fixed_size: 0
    .sgpr_count:     28
    .sgpr_spill_count: 0
    .symbol:         _Z5k_decPKiPKDF16_S2_PKfS4_S4_Pf.kd
    .uniform_work_group_size: 1
    .uses_dynamic_stack: false
    .vgpr_count:     248
    .vgpr_spill_count: 0
    .wavefront_size: 64
  - .agpr_count:     0
    .args:
      - .actual_access:  read_only
        .address_space:  global
        .offset:         0
        .size:           8
        .value_kind:     global_buffer
      - .actual_access:  read_only
        .address_space:  global
        .offset:         8
        .size:           8
        .value_kind:     global_buffer
      - .actual_access:  read_only
        .address_space:  global
        .offset:         16
        .size:           8
        .value_kind:     global_buffer
      - .actual_access:  read_only
        .address_space:  global
        .offset:         24
        .size:           8
        .value_kind:     global_buffer
      - .actual_access:  read_only
        .address_space:  global
        .offset:         32
        .size:           8
        .value_kind:     global_buffer
      - .actual_access:  read_only
        .address_space:  global
        .offset:         40
        .size:           8
        .value_kind:     global_buffer
      - .actual_access:  write_only
        .address_space:  global
        .offset:         48
        .size:           8
        .value_kind:     global_buffer
      - .actual_access:  read_only
        .address_space:  global
        .offset:         56
        .size:           8
        .value_kind:     global_buffer
    .group_segment_fixed_size: 0
    .kernarg_segment_align: 8
    .kernarg_segment_size: 64
    .language:       OpenCL C
    .language_version:
      - 2
      - 0
    .max_flat_workgroup_size: 64
    .name:           _Z5k_aggILi1EEvPKiS1_S1_PKDv4_jPKfS6_PS2_PDF16_
    .private_segment_fixed_size: 0
    .sgpr_count:     82
    .sgpr_spill_count: 0
    .symbol:         _Z5k_aggILi1EEvPKiS1_S1_PKDv4_jPKfS6_PS2_PDF16_.kd
    .uniform_work_group_size: 1
    .uses_dynamic_stack: false
    .vgpr_count:     72
    .vgpr_spill_count: 0
    .wavefront_size: 64
  - .agpr_count:     0
    .args:
      - .actual_access:  read_only
        .address_space:  global
        .offset:         0
        .size:           8
        .value_kind:     global_buffer
      - .actual_access:  read_only
        .address_space:  global
        .offset:         8
        .size:           8
        .value_kind:     global_buffer
      - .actual_access:  read_only
        .address_space:  global
        .offset:         16
        .size:           8
        .value_kind:     global_buffer
      - .actual_access:  read_only
        .address_space:  global
        .offset:         24
        .size:           8
        .value_kind:     global_buffer
      - .actual_access:  read_only
        .address_space:  global
        .offset:         32
        .size:           8
        .value_kind:     global_buffer
      - .actual_access:  read_only
        .address_space:  global
        .offset:         40
        .size:           8
        .value_kind:     global_buffer
      - .actual_access:  read_only
        .address_space:  global
        .offset:         48
        .size:           8
        .value_kind:     global_buffer
      - .actual_access:  write_only
        .address_space:  global
        .offset:         56
        .size:           8
        .value_kind:     global_buffer
    .group_segment_fixed_size: 0
    .kernarg_segment_align: 8
    .kernarg_segment_size: 64
    .language:       OpenCL C
    .language_version:
      - 2
      - 0
    .max_flat_workgroup_size: 64
    .name:           _Z5k_aggILi2EEvPKiS1_S1_PKDv4_jPKfS6_PS2_PDF16_
    .private_segment_fixed_size: 0
    .sgpr_count:     66
    .sgpr_spill_count: 0
    .symbol:         _Z5k_aggILi2EEvPKiS1_S1_PKDv4_jPKfS6_PS2_PDF16_.kd
    .uniform_work_group_size: 1
    .uses_dynamic_stack: false
    .vgpr_count:     72
    .vgpr_spill_count: 0
    .wavefront_size: 64
